# v63 + layer-0 mixers load balance: the 8 WGs running the context Fourier GEMM give their 2 conv units to WGs 104..119 (third trip)
# speedup vs baseline: 1.0103x; 1.0103x over previous
; DI KParamsPtr kparams() { KParamsPtr p = (KParamsPtr)__builtin_amdgcn_kernarg_segment_ptr(); asm volatile("" : "+s"(p)); return p; }
; template <int li>
; DI void layer_phases(unsigned char* smem, LAS unsigned char* ldsL, const int lo, const int hi) {
;     ...
;             for (int srep_ = 0; srep_ < NSUB(6); ++srep_) if (SUBEN(6)) { KParamsPtr kp = kparams(); unsigned char* ws = kp->ws; const int G = gridDim.x;
;               for (int it = 0; ; ++it) {
;                 int L = (int)blockIdx.x + it * G;
;                 if (G == 256 && it == 2) { const int j = (int)blockIdx.x - 64; if (j < 0 || j >= 32) break; L = 512 + j; }
;                 if (L >= (li == DEPTH - 1 ? 512 : 512 + 32)) break;
;                 int seqrow, Ls, t0;
;                 if (L < 512) { seqrow = (L >> 6) * SEQ; Ls = SEQ; t0 = (L & 63) * 64; } else { const int j = L - 512; seqrow = NLAT + (j >> 2) * CTX; Ls = CTX; t0 = (j & 3) * 64; }
;                 conv_unit(smem, seqrow, Ls, t0, WSP(const bf16_t, WS_BU), WSP(const bf16_t, WS_BG), kp->conv_w + li * 31 * 256, kp->conv_b + li * 256, kp->conv_lg + li * 256, kp->conv_lb + li * 256, WSP(unsigned char, WS_CAT));
;               } }
.LBB0_732:
	s_mov_b64 s[4:5], s[0:1]
	s_andn2_b64 vcc, exec, s[20:21]
	s_cbranch_vccnz .LBB0_846
	s_load_dwordx2 s[54:55], s[4:5], 0xd8
	s_load_dwordx8 s[36:43], s[4:5], 0x58
	s_mov_b32 s28, 0
	s_movk_i32 s29, 0xfc0
	s_movk_i32 s46, 0x1000
	s_waitcnt lgkmcnt(0)
	s_add_u32 s56, s54, 0x22e54000
	s_addc_u32 s57, s55, 0
	s_add_u32 s58, s54, 0x23f54000
	s_addc_u32 s59, s55, 0
	v_mov_b32_e32 v59, 0
	s_movk_i32 s47, 0xbc0
	s_movk_i32 s48, 0x9c0
	s_movk_i32 s49, 0x7c0
	s_movk_i32 s65, 0x5c0
	s_movk_i32 s66, 0x3c0
	s_movk_i32 s67, 0x1c0
	v_mov_b32_e32 v62, 0x358637bd
	s_mov_b32 s68, 0x800000
	s_mov_b32 s69, 0xc3e00000
	v_mov_b32_e32 v63, 0x43e00000
	s_sub_i32 s74, s2, 0x60
	s_cmp_lt_u32 s74, 8
	s_cbranch_scc1 .LBB0_846
	s_movk_i32 s75, 0x1c0
	s_mov_b64 s[82:83], s[44:45]
	s_sub_i32 s74, s2, 0x68
	s_cmp_lt_u32 s74, 8
	s_cselect_b32 s75, -8, s75
	s_cselect_b64 s[82:83], 0, s[82:83]
	s_sub_i32 s74, s2, 0x70
	s_cmp_lt_u32 s74, 8
	s_cselect_b32 s75, 0xf0, s75
	s_cselect_b64 s[82:83], 0, s[82:83]
	s_mov_b32 s4, s2
	s_branch .LBB0_735
.LBB0_734:
	s_or_b64 exec, exec, s[10:11]
	s_add_i32 s28, s28, 1
	s_cmp_eq_u32 s28, 2
	s_cselect_b64 s[4:5], -1, 0
	s_and_b64 s[4:5], s[52:53], s[4:5]
	s_and_b64 s[6:7], s[82:83], s[4:5]
	s_mul_i32 s8, s28, s64
	s_and_b64 s[4:5], s[4:5], exec
	s_cselect_b32 s4, s75, s8
	s_add_i32 s4, s4, s2
	s_cmpk_gt_i32 s4, 0x21f
	s_cselect_b64 s[8:9], -1, 0
	s_or_b64 s[6:7], s[6:7], s[8:9]
	s_andn2_b64 vcc, exec, s[6:7]
	s_barrier
	s_cbranch_vccz .LBB0_846
